# P13 and P15 gather loops: vmcnt(0) before each batch of table gathers (fewer loads in flight per wave)
# baseline (speedup 1.0000x reference)
.LBB0_1585:
	ds_read2_b32 v[10:11], v145 offset1:4
	global_load_dwordx2 v[140:141], v[138:139], off
	ds_read2_b32 v[12:13], v145 offset0:8 offset1:12
	ds_read_b128 v[86:89], v144 offset:512
	ds_read_b128 v[14:17], v144 offset:528
	ds_read_b128 v[6:9], v144 offset:544
	ds_read_b128 v[2:5], v144 offset:560
	s_waitcnt lgkmcnt(3)
	v_bfe_u32 v86, v86, v146, 8
	v_ashrrev_i32_e32 v19, 31, v10
	v_mov_b32_e32 v18, v10
	v_lshlrev_b64 v[18:19], 8, v[18:19]
	v_ashrrev_i32_e32 v21, 31, v11
	v_mov_b32_e32 v20, v11
	v_lshl_add_u64 v[18:19], v[136:137], 0, v[18:19]
	v_lshlrev_b64 v[10:11], 8, v[20:21]
	v_lshl_add_u64 v[10:11], v[136:137], 0, v[10:11]
	s_waitcnt vmcnt(0)
	global_load_dwordx4 v[118:121], v[18:19], off
	global_load_dwordx4 v[106:109], v[10:11], off
	v_ashrrev_i32_e32 v11, 31, v12
	v_mov_b32_e32 v10, v12
	v_lshlrev_b64 v[10:11], 8, v[10:11]
	v_ashrrev_i32_e32 v19, 31, v13
	v_mov_b32_e32 v18, v13
	v_lshl_add_u64 v[10:11], v[136:137], 0, v[10:11]
	v_lshlrev_b64 v[18:19], 8, v[18:19]
	ds_read2_b32 v[12:13], v145 offset0:16 offset1:20
	v_lshl_add_u64 v[18:19], v[136:137], 0, v[18:19]
	global_load_dwordx4 v[114:117], v[10:11], off
	global_load_dwordx4 v[98:101], v[18:19], off
	v_lshlrev_b32_e32 v86, v1, v86
	v_cndmask_b32_e64 v150, 0, v86, s[12:13]
	s_waitcnt lgkmcnt(0)
	v_ashrrev_i32_e32 v11, 31, v12
	v_mov_b32_e32 v10, v12
	v_lshlrev_b64 v[10:11], 8, v[10:11]
	v_ashrrev_i32_e32 v19, 31, v13
	v_mov_b32_e32 v18, v13
	v_lshl_add_u64 v[10:11], v[136:137], 0, v[10:11]
	v_lshlrev_b64 v[18:19], 8, v[18:19]
	ds_read2_b32 v[12:13], v145 offset0:24 offset1:28
	v_lshl_add_u64 v[18:19], v[136:137], 0, v[18:19]
	s_waitcnt vmcnt(0)
	global_load_dwordx4 v[110:113], v[10:11], off
	global_load_dwordx4 v[90:93], v[18:19], off
	v_cndmask_b32_e64 v151, 0, v86, s[14:15]
	v_bfe_u32 v14, v14, v146, 8
	s_waitcnt lgkmcnt(0)
	v_ashrrev_i32_e32 v11, 31, v12
	v_mov_b32_e32 v10, v12
	v_lshlrev_b64 v[10:11], 8, v[10:11]
	v_ashrrev_i32_e32 v19, 31, v13
	v_mov_b32_e32 v18, v13
	v_lshl_add_u64 v[10:11], v[136:137], 0, v[10:11]
	v_lshlrev_b64 v[18:19], 8, v[18:19]
	ds_read2_b32 v[12:13], v145 offset0:32 offset1:36
	v_lshl_add_u64 v[18:19], v[136:137], 0, v[18:19]
	s_waitcnt vmcnt(0)
	global_load_dwordx4 v[102:105], v[10:11], off
	global_load_dwordx4 v[82:85], v[18:19], off
	v_lshlrev_b32_e32 v14, v1, v14
	v_bfe_u32 v6, v6, v146, 8
	s_waitcnt lgkmcnt(0)
	v_ashrrev_i32_e32 v11, 31, v12
	v_mov_b32_e32 v10, v12
	v_lshlrev_b64 v[10:11], 8, v[10:11]
	v_ashrrev_i32_e32 v19, 31, v13
	v_mov_b32_e32 v18, v13
	v_lshl_add_u64 v[10:11], v[136:137], 0, v[10:11]
	v_lshlrev_b64 v[18:19], 8, v[18:19]
	ds_read2_b32 v[12:13], v145 offset0:40 offset1:44
	v_lshl_add_u64 v[18:19], v[136:137], 0, v[18:19]
	s_waitcnt vmcnt(0)
	global_load_dwordx4 v[94:97], v[10:11], off
	global_load_dwordx4 v[74:77], v[18:19], off
	v_lshlrev_b32_e32 v6, v1, v6
	v_bfe_u32 v2, v2, v146, 8
	s_waitcnt lgkmcnt(0)
	v_ashrrev_i32_e32 v11, 31, v12
	v_mov_b32_e32 v10, v12
	v_lshlrev_b64 v[10:11], 8, v[10:11]
	v_ashrrev_i32_e32 v19, 31, v13
	v_mov_b32_e32 v18, v13
	v_lshl_add_u64 v[10:11], v[136:137], 0, v[10:11]
	ds_read2_b32 v[12:13], v145 offset0:48 offset1:52
	v_lshlrev_b64 v[18:19], 8, v[18:19]
	v_lshl_add_u64 v[18:19], v[136:137], 0, v[18:19]
	s_waitcnt vmcnt(0)
	global_load_dwordx4 v[78:81], v[10:11], off
	global_load_dwordx4 v[66:69], v[18:19], off
	v_lshlrev_b32_e32 v2, v1, v2
	s_waitcnt lgkmcnt(0)
	v_ashrrev_i32_e32 v11, 31, v12
	v_mov_b32_e32 v10, v12
	v_ashrrev_i32_e32 v19, 31, v13
	v_mov_b32_e32 v18, v13
	ds_read2_b32 v[12:13], v145 offset0:56 offset1:60
	v_lshlrev_b64 v[10:11], 8, v[10:11]
	v_lshlrev_b64 v[18:19], 8, v[18:19]
	v_lshl_add_u64 v[10:11], v[136:137], 0, v[10:11]
	v_lshl_add_u64 v[18:19], v[136:137], 0, v[18:19]
	global_load_dwordx4 v[70:73], v[10:11], off
	global_load_dwordx4 v[58:61], v[18:19], off
	s_waitcnt lgkmcnt(0)
	v_ashrrev_i32_e32 v11, 31, v12
	v_mov_b32_e32 v10, v12
	v_ashrrev_i32_e32 v19, 31, v13
	v_mov_b32_e32 v18, v13
	ds_read2_b32 v[12:13], v145 offset0:64 offset1:68
	v_lshlrev_b64 v[10:11], 8, v[10:11]
	v_lshl_add_u64 v[10:11], v[136:137], 0, v[10:11]
	v_lshlrev_b64 v[18:19], 8, v[18:19]
	v_lshl_add_u64 v[18:19], v[136:137], 0, v[18:19]
	global_load_dwordx4 v[62:65], v[10:11], off
	global_load_dwordx4 v[46:49], v[18:19], off
	s_waitcnt lgkmcnt(0)
	v_ashrrev_i32_e32 v11, 31, v12
	v_mov_b32_e32 v10, v12
	v_lshlrev_b64 v[10:11], 8, v[10:11]
	v_ashrrev_i32_e32 v19, 31, v13
	v_mov_b32_e32 v18, v13
	v_lshl_add_u64 v[10:11], v[136:137], 0, v[10:11]
	ds_read2_b32 v[12:13], v145 offset0:72 offset1:76
	v_lshlrev_b64 v[18:19], 8, v[18:19]
	v_lshl_add_u64 v[18:19], v[136:137], 0, v[18:19]
	global_load_dwordx4 v[50:53], v[10:11], off
	global_load_dwordx4 v[38:41], v[18:19], off
	ds_read2_b32 v[20:21], v145 offset0:80 offset1:84
	s_waitcnt lgkmcnt(1)
	v_ashrrev_i32_e32 v19, 31, v13
	v_mov_b32_e32 v18, v13
	v_ashrrev_i32_e32 v11, 31, v12
	v_mov_b32_e32 v10, v12
	v_lshlrev_b64 v[12:13], 8, v[18:19]
	s_waitcnt lgkmcnt(0)
	v_ashrrev_i32_e32 v19, 31, v20
	v_mov_b32_e32 v18, v20
	v_ashrrev_i32_e32 v23, 31, v21
	v_mov_b32_e32 v22, v21
	v_lshlrev_b64 v[10:11], 8, v[10:11]
	v_lshlrev_b64 v[18:19], 8, v[18:19]
	v_lshlrev_b64 v[22:23], 8, v[22:23]
	v_lshl_add_u64 v[10:11], v[136:137], 0, v[10:11]
	v_lshl_add_u64 v[12:13], v[136:137], 0, v[12:13]
	v_lshl_add_u64 v[18:19], v[136:137], 0, v[18:19]
	v_lshl_add_u64 v[22:23], v[136:137], 0, v[22:23]
	s_waitcnt vmcnt(0)
	global_load_dwordx4 v[42:45], v[10:11], off
	global_load_dwordx4 v[30:33], v[12:13], off
	ds_read_b128 v[54:57], v144 offset:576
	ds_read_b128 v[10:13], v144 offset:592
	ds_read2_b32 v[20:21], v145 offset0:88 offset1:92
	global_load_dwordx4 v[34:37], v[18:19], off
	s_nop 0
	global_load_dwordx4 v[22:25], v[22:23], off
	ds_read2_b32 v[152:153], v145 offset0:96 offset1:100
	s_waitcnt lgkmcnt(2)
	v_bfe_u32 v10, v10, v146, 8
	s_waitcnt lgkmcnt(1)
	v_ashrrev_i32_e32 v19, 31, v20
	v_mov_b32_e32 v18, v20
	s_waitcnt lgkmcnt(0)
	v_ashrrev_i32_e32 v149, 31, v152
	v_mov_b32_e32 v148, v152
	v_lshlrev_b64 v[148:149], 8, v[148:149]
	v_lshl_add_u64 v[156:157], v[136:137], 0, v[148:149]
	v_cndmask_b32_e64 v148, 0, v86, s[8:9]
	v_cndmask_b32_e64 v149, 0, v86, s[10:11]
	v_bfe_u32 v86, v87, v146, 8
	v_lshlrev_b32_e32 v86, v1, v86
	s_waitcnt vmcnt(21)
	v_mfma_i32_16x16x64_i8 v[118:121], v[148:151], v[118:121], 0
	v_cndmask_b32_e64 v148, 0, v86, s[8:9]
	v_cndmask_b32_e64 v149, 0, v86, s[10:11]
	v_cndmask_b32_e64 v150, 0, v86, s[12:13]
	v_cndmask_b32_e64 v151, 0, v86, s[14:15]
	v_ashrrev_i32_e32 v155, 31, v153
	v_mov_b32_e32 v154, v153
	v_bfe_u32 v86, v88, v146, 8
	v_lshlrev_b64 v[152:153], 8, v[154:155]
	v_lshlrev_b32_e32 v86, v1, v86
	v_lshl_add_u64 v[158:159], v[136:137], 0, v[152:153]
	v_cndmask_b32_e64 v152, 0, v86, s[8:9]
	v_cndmask_b32_e64 v153, 0, v86, s[10:11]
	v_cndmask_b32_e64 v154, 0, v86, s[12:13]
	v_cndmask_b32_e64 v155, 0, v86, s[14:15]
	s_waitcnt vmcnt(20)
	v_mfma_i32_16x16x64_i8 v[148:151], v[148:151], v[106:109], v[118:121]
	v_bfe_u32 v86, v89, v146, 8
	v_ashrrev_i32_e32 v27, 31, v21
	v_mov_b32_e32 v26, v21
	v_lshlrev_b32_e32 v89, v1, v86
	v_lshlrev_b64 v[18:19], 8, v[18:19]
	v_lshlrev_b64 v[20:21], 8, v[26:27]
	v_cndmask_b32_e64 v86, 0, v89, s[8:9]
	v_cndmask_b32_e64 v87, 0, v89, s[10:11]
	v_cndmask_b32_e64 v88, 0, v89, s[12:13]
	v_cndmask_b32_e64 v89, 0, v89, s[14:15]
	v_lshl_add_u64 v[18:19], v[136:137], 0, v[18:19]
	v_lshl_add_u64 v[20:21], v[136:137], 0, v[20:21]
	s_waitcnt vmcnt(19)
	v_mfma_i32_16x16x64_i8 v[114:117], v[152:155], v[114:117], v[148:151]
	s_waitcnt vmcnt(0)
	global_load_dwordx4 v[26:29], v[18:19], off
	s_nop 0
	global_load_dwordx4 v[18:21], v[20:21], off
	s_nop 0
	global_load_dwordx4 v[118:121], v[156:157], off
	global_load_dwordx4 v[106:109], v[158:159], off
	ds_read2_b32 v[156:157], v145 offset0:104 offset1:108
	v_cndmask_b32_e64 v148, 0, v14, s[8:9]
	v_cndmask_b32_e64 v149, 0, v14, s[10:11]
	v_cndmask_b32_e64 v150, 0, v14, s[12:13]
	v_cndmask_b32_e64 v151, 0, v14, s[14:15]
	s_waitcnt vmcnt(22)
	v_mfma_i32_16x16x64_i8 v[86:89], v[86:89], v[98:101], v[114:117]
	v_bfe_u32 v14, v15, v146, 8
	s_waitcnt lgkmcnt(0)
	v_ashrrev_i32_e32 v99, 31, v156
	v_mov_b32_e32 v98, v156
	v_lshlrev_b32_e32 v14, v1, v14
	v_lshlrev_b64 v[114:115], 8, v[98:99]
	v_cndmask_b32_e64 v98, 0, v14, s[8:9]
	v_cndmask_b32_e64 v99, 0, v14, s[10:11]
	v_cndmask_b32_e64 v100, 0, v14, s[12:13]
	v_cndmask_b32_e64 v101, 0, v14, s[14:15]
	s_waitcnt vmcnt(21)
	v_mfma_i32_16x16x64_i8 v[86:89], v[148:151], v[110:113], v[86:89]
	v_bfe_u32 v14, v16, v146, 8
	v_lshlrev_b32_e32 v14, v1, v14
	v_cndmask_b32_e64 v110, 0, v14, s[8:9]
	v_cndmask_b32_e64 v111, 0, v14, s[10:11]
	v_cndmask_b32_e64 v112, 0, v14, s[12:13]
	v_cndmask_b32_e64 v113, 0, v14, s[14:15]
	s_waitcnt vmcnt(20)
	v_mfma_i32_16x16x64_i8 v[86:89], v[98:101], v[90:93], v[86:89]
	v_bfe_u32 v14, v17, v146, 8
	v_lshlrev_b32_e32 v17, v1, v14
	v_cndmask_b32_e64 v14, 0, v17, s[8:9]
	v_cndmask_b32_e64 v15, 0, v17, s[10:11]
	v_cndmask_b32_e64 v16, 0, v17, s[12:13]
	v_cndmask_b32_e64 v17, 0, v17, s[14:15]
	s_waitcnt vmcnt(19)
	v_mfma_i32_16x16x64_i8 v[86:89], v[110:113], v[102:105], v[86:89]
	v_cndmask_b32_e64 v90, 0, v6, s[8:9]
	v_cndmask_b32_e64 v91, 0, v6, s[10:11]
	v_cndmask_b32_e64 v92, 0, v6, s[12:13]
	v_cndmask_b32_e64 v93, 0, v6, s[14:15]
	s_waitcnt vmcnt(18)
	v_mfma_i32_16x16x64_i8 v[14:17], v[14:17], v[82:85], v[86:89]
	v_ashrrev_i32_e32 v101, 31, v157
	v_mov_b32_e32 v100, v157
	v_bfe_u32 v6, v7, v146, 8
	v_lshlrev_b64 v[82:83], 8, v[100:101]
	v_lshlrev_b32_e32 v6, v1, v6
	v_lshl_add_u64 v[100:101], v[136:137], 0, v[82:83]
	v_cndmask_b32_e64 v82, 0, v6, s[8:9]
	v_cndmask_b32_e64 v83, 0, v6, s[10:11]
	v_cndmask_b32_e64 v84, 0, v6, s[12:13]
	v_cndmask_b32_e64 v85, 0, v6, s[14:15]
	s_waitcnt vmcnt(17)
	v_mfma_i32_16x16x64_i8 v[14:17], v[90:93], v[94:97], v[14:17]
	v_bfe_u32 v6, v8, v146, 8
	v_lshlrev_b32_e32 v6, v1, v6
	ds_read2_b32 v[102:103], v145 offset0:112 offset1:116
	s_waitcnt vmcnt(16)
	v_mfma_i32_16x16x64_i8 v[14:17], v[82:85], v[74:77], v[14:17]
	v_cndmask_b32_e64 v74, 0, v6, s[8:9]
	v_cndmask_b32_e64 v75, 0, v6, s[10:11]
	v_cndmask_b32_e64 v76, 0, v6, s[12:13]
	v_cndmask_b32_e64 v77, 0, v6, s[14:15]
	v_bfe_u32 v6, v9, v146, 8
	v_lshlrev_b32_e32 v9, v1, v6
	v_cndmask_b32_e64 v6, 0, v9, s[8:9]
	v_cndmask_b32_e64 v7, 0, v9, s[10:11]
	v_cndmask_b32_e64 v8, 0, v9, s[12:13]
	v_cndmask_b32_e64 v9, 0, v9, s[14:15]
	s_waitcnt vmcnt(15)
	v_mfma_i32_16x16x64_i8 v[14:17], v[74:77], v[78:81], v[14:17]
	v_lshl_add_u64 v[98:99], v[136:137], 0, v[114:115]
	s_waitcnt vmcnt(0)
	global_load_dwordx4 v[86:89], v[98:99], off
	global_load_dwordx4 v[90:93], v[100:101], off
	ds_read_b128 v[74:77], v144 offset:608
	ds_read_b128 v[78:81], v144 offset:624
	s_waitcnt vmcnt(16)
	v_mfma_i32_16x16x64_i8 v[6:9], v[6:9], v[66:69], v[14:17]
	s_waitcnt lgkmcnt(2)
	v_ashrrev_i32_e32 v95, 31, v102
	v_mov_b32_e32 v94, v102
	v_lshlrev_b64 v[82:83], 8, v[94:95]
	v_cndmask_b32_e64 v14, 0, v2, s[8:9]
	v_cndmask_b32_e64 v15, 0, v2, s[10:11]
	v_cndmask_b32_e64 v16, 0, v2, s[12:13]
	v_cndmask_b32_e64 v17, 0, v2, s[14:15]
	v_bfe_u32 v2, v3, v146, 8
	v_lshlrev_b32_e32 v2, v1, v2
	v_cndmask_b32_e64 v66, 0, v2, s[8:9]
	v_cndmask_b32_e64 v67, 0, v2, s[10:11]
	v_cndmask_b32_e64 v68, 0, v2, s[12:13]
	v_cndmask_b32_e64 v69, 0, v2, s[14:15]
	s_waitcnt vmcnt(15)
	v_mfma_i32_16x16x64_i8 v[6:9], v[14:17], v[70:73], v[6:9]
	v_bfe_u32 v2, v4, v146, 8
	v_lshlrev_b32_e32 v2, v1, v2
	v_cndmask_b32_e64 v14, 0, v2, s[8:9]
	v_cndmask_b32_e64 v15, 0, v2, s[10:11]
	v_cndmask_b32_e64 v16, 0, v2, s[12:13]
	v_cndmask_b32_e64 v17, 0, v2, s[14:15]
	s_waitcnt vmcnt(14)
	v_mfma_i32_16x16x64_i8 v[6:9], v[66:69], v[58:61], v[6:9]
	v_bfe_u32 v2, v5, v146, 8
	v_lshlrev_b32_e32 v5, v1, v2
	v_cndmask_b32_e64 v2, 0, v5, s[8:9]
	v_cndmask_b32_e64 v3, 0, v5, s[10:11]
	v_cndmask_b32_e64 v4, 0, v5, s[12:13]
	v_cndmask_b32_e64 v5, 0, v5, s[14:15]
	s_waitcnt vmcnt(13)
	v_mfma_i32_16x16x64_i8 v[6:9], v[14:17], v[62:65], v[6:9]
	v_ashrrev_i32_e32 v73, 31, v103
	v_mov_b32_e32 v72, v103
	v_lshlrev_b64 v[14:15], 8, v[72:73]
	s_waitcnt vmcnt(12)
	v_mfma_i32_16x16x64_i8 v[2:5], v[2:5], v[46:49], v[6:9]
	v_lshl_add_u64 v[58:59], v[136:137], 0, v[14:15]
	v_bfe_u32 v14, v55, v146, 8
	v_lshlrev_b32_e32 v17, v1, v14
	v_bfe_u32 v6, v54, v146, 8
	v_lshlrev_b32_e32 v9, v1, v6
	v_cndmask_b32_e64 v6, 0, v9, s[8:9]
	v_cndmask_b32_e64 v7, 0, v9, s[10:11]
	v_cndmask_b32_e64 v8, 0, v9, s[12:13]
	v_cndmask_b32_e64 v9, 0, v9, s[14:15]
	v_cndmask_b32_e64 v14, 0, v17, s[8:9]
	v_cndmask_b32_e64 v15, 0, v17, s[10:11]
	v_cndmask_b32_e64 v16, 0, v17, s[12:13]
	v_cndmask_b32_e64 v17, 0, v17, s[14:15]
	s_waitcnt vmcnt(11)
	v_mfma_i32_16x16x64_i8 v[2:5], v[6:9], v[50:53], v[2:5]
	ds_read2_b32 v[60:61], v145 offset0:120 offset1:124
	v_lshl_add_u64 v[70:71], v[136:137], 0, v[82:83]
	s_waitcnt vmcnt(0)
	global_load_dwordx4 v[6:9], v[70:71], off
	global_load_dwordx4 v[46:49], v[58:59], off
	s_waitcnt vmcnt(12)
	v_mfma_i32_16x16x64_i8 v[2:5], v[14:17], v[38:41], v[2:5]
	v_bfe_u32 v14, v56, v146, 8
	v_lshlrev_b32_e32 v17, v1, v14
	v_cndmask_b32_e64 v14, 0, v17, s[8:9]
	v_cndmask_b32_e64 v15, 0, v17, s[10:11]
	v_cndmask_b32_e64 v16, 0, v17, s[12:13]
	v_cndmask_b32_e64 v17, 0, v17, s[14:15]
	v_bfe_u32 v38, v57, v146, 8
	v_lshlrev_b32_e32 v41, v1, v38
	v_cndmask_b32_e64 v38, 0, v41, s[8:9]
	v_cndmask_b32_e64 v39, 0, v41, s[10:11]
	v_cndmask_b32_e64 v40, 0, v41, s[12:13]
	v_cndmask_b32_e64 v41, 0, v41, s[14:15]
	s_waitcnt vmcnt(11)
	v_mfma_i32_16x16x64_i8 v[2:5], v[14:17], v[42:45], v[2:5]
	s_waitcnt lgkmcnt(0)
	v_ashrrev_i32_e32 v51, 31, v60
	v_mov_b32_e32 v50, v60
	v_lshlrev_b64 v[14:15], 8, v[50:51]
	v_lshlrev_b32_e32 v10, v1, v10
	v_lshl_add_u64 v[42:43], v[136:137], 0, v[14:15]
	v_cndmask_b32_e64 v14, 0, v10, s[8:9]
	v_cndmask_b32_e64 v15, 0, v10, s[10:11]
	v_cndmask_b32_e64 v16, 0, v10, s[12:13]
	v_cndmask_b32_e64 v17, 0, v10, s[14:15]
	s_waitcnt vmcnt(10)
	v_mfma_i32_16x16x64_i8 v[2:5], v[38:41], v[30:33], v[2:5]
	v_bfe_u32 v10, v11, v146, 8
	v_lshlrev_b32_e32 v10, v1, v10
	v_cndmask_b32_e64 v30, 0, v10, s[8:9]
	v_cndmask_b32_e64 v31, 0, v10, s[10:11]
	v_cndmask_b32_e64 v32, 0, v10, s[12:13]
	v_cndmask_b32_e64 v33, 0, v10, s[14:15]
	s_waitcnt vmcnt(9)
	v_mfma_i32_16x16x64_i8 v[2:5], v[14:17], v[34:37], v[2:5]
	v_ashrrev_i32_e32 v11, 31, v61
	v_mov_b32_e32 v10, v61
	v_lshlrev_b64 v[34:35], 8, v[10:11]
	v_bfe_u32 v10, v12, v146, 8
	v_lshlrev_b32_e32 v10, v1, v10
	v_cndmask_b32_e64 v14, 0, v10, s[8:9]
	v_cndmask_b32_e64 v15, 0, v10, s[10:11]
	v_cndmask_b32_e64 v16, 0, v10, s[12:13]
	v_cndmask_b32_e64 v17, 0, v10, s[14:15]
	s_waitcnt vmcnt(8)
	v_mfma_i32_16x16x64_i8 v[2:5], v[30:33], v[22:25], v[2:5]
	v_lshl_add_u64 v[22:23], v[136:137], 0, v[34:35]
	v_bfe_u32 v10, v13, v146, 8
	v_lshlrev_b32_e32 v13, v1, v10
	s_waitcnt vmcnt(7)
	v_mfma_i32_16x16x64_i8 v[2:5], v[14:17], v[26:29], v[2:5]
	s_waitcnt vmcnt(0)
	global_load_dwordx4 v[14:17], v[42:43], off
	s_nop 0
	global_load_dwordx4 v[22:25], v[22:23], off
	v_cndmask_b32_e64 v10, 0, v13, s[8:9]
	v_cndmask_b32_e64 v11, 0, v13, s[10:11]
	v_cndmask_b32_e64 v12, 0, v13, s[12:13]
	v_cndmask_b32_e64 v13, 0, v13, s[14:15]
	s_waitcnt vmcnt(8)
	s_nop 0
	v_mfma_i32_16x16x64_i8 v[2:5], v[10:13], v[18:21], v[2:5]
	global_load_dword v18, v123, s[28:29]
	v_bfe_u32 v10, v74, v146, 8
	v_lshlrev_b32_e32 v13, v1, v10
	v_cndmask_b32_e64 v10, 0, v13, s[8:9]
	v_cndmask_b32_e64 v11, 0, v13, s[10:11]
	v_cndmask_b32_e64 v12, 0, v13, s[12:13]
	v_cndmask_b32_e64 v13, 0, v13, s[14:15]
	v_lshlrev_b32_e32 v19, 16, v140
	s_add_u32 s28, s28, s22
	s_waitcnt vmcnt(8)
	v_mfma_i32_16x16x64_i8 v[2:5], v[10:13], v[118:121], v[2:5]
	v_bfe_u32 v10, v75, v146, 8
	v_lshlrev_b32_e32 v13, v1, v10
	v_cndmask_b32_e64 v10, 0, v13, s[8:9]
	v_cndmask_b32_e64 v11, 0, v13, s[10:11]
	v_cndmask_b32_e64 v12, 0, v13, s[12:13]
	v_cndmask_b32_e64 v13, 0, v13, s[14:15]
	s_addc_u32 s29, s29, s23
	s_andn2_b64 vcc, exec, s[34:35]
	s_waitcnt vmcnt(7)
	v_mfma_i32_16x16x64_i8 v[2:5], v[10:13], v[106:109], v[2:5]
	v_bfe_u32 v10, v76, v146, 8
	v_lshlrev_b32_e32 v13, v1, v10
	v_cndmask_b32_e64 v10, 0, v13, s[8:9]
	v_cndmask_b32_e64 v11, 0, v13, s[10:11]
	v_cndmask_b32_e64 v12, 0, v13, s[12:13]
	v_cndmask_b32_e64 v13, 0, v13, s[14:15]
	s_waitcnt vmcnt(6)
	s_nop 0
	v_mfma_i32_16x16x64_i8 v[2:5], v[10:13], v[86:89], v[2:5]
	v_bfe_u32 v10, v77, v146, 8
	v_lshlrev_b32_e32 v13, v1, v10
	v_cndmask_b32_e64 v10, 0, v13, s[8:9]
	v_cndmask_b32_e64 v11, 0, v13, s[10:11]
	v_cndmask_b32_e64 v12, 0, v13, s[12:13]
	v_cndmask_b32_e64 v13, 0, v13, s[14:15]
	s_waitcnt vmcnt(5)
	s_nop 0
	v_mfma_i32_16x16x64_i8 v[2:5], v[10:13], v[90:93], v[2:5]
	v_bfe_u32 v10, v78, v146, 8
	v_lshlrev_b32_e32 v13, v1, v10
	v_cndmask_b32_e64 v10, 0, v13, s[8:9]
	v_cndmask_b32_e64 v11, 0, v13, s[10:11]
	v_cndmask_b32_e64 v12, 0, v13, s[12:13]
	v_cndmask_b32_e64 v13, 0, v13, s[14:15]
	s_waitcnt vmcnt(4)
	s_nop 0
	v_mfma_i32_16x16x64_i8 v[2:5], v[10:13], v[6:9], v[2:5]
	v_bfe_u32 v6, v79, v146, 8
	v_lshlrev_b32_e32 v9, v1, v6
	v_cndmask_b32_e64 v6, 0, v9, s[8:9]
	v_cndmask_b32_e64 v7, 0, v9, s[10:11]
	v_cndmask_b32_e64 v8, 0, v9, s[12:13]
	v_cndmask_b32_e64 v9, 0, v9, s[14:15]
	v_bfe_u32 v10, v81, v146, 8
	v_lshlrev_b32_e32 v13, v1, v10
	s_waitcnt vmcnt(3)
	v_mfma_i32_16x16x64_i8 v[2:5], v[6:9], v[46:49], v[2:5]
	v_bfe_u32 v6, v80, v146, 8
	v_lshlrev_b32_e32 v9, v1, v6
	v_cndmask_b32_e64 v6, 0, v9, s[8:9]
	v_cndmask_b32_e64 v7, 0, v9, s[10:11]
	v_cndmask_b32_e64 v8, 0, v9, s[12:13]
	v_cndmask_b32_e64 v9, 0, v9, s[14:15]
	v_cndmask_b32_e64 v10, 0, v13, s[8:9]
	v_cndmask_b32_e64 v11, 0, v13, s[10:11]
	v_cndmask_b32_e64 v12, 0, v13, s[12:13]
	v_cndmask_b32_e64 v13, 0, v13, s[14:15]
	s_waitcnt vmcnt(2)
	v_mfma_i32_16x16x64_i8 v[2:5], v[6:9], v[14:17], v[2:5]
	v_and_b32_e32 v6, 0xffff0000, v140
	v_lshlrev_b32_e32 v7, 16, v141
	v_and_b32_e32 v8, 0xffff0000, v141
	s_waitcnt vmcnt(1)
	v_mfma_i32_16x16x64_i8 v[2:5], v[10:13], v[22:25], v[2:5]
	s_nop 7
	v_cvt_f32_i32_e32 v2, v2
	v_cvt_f32_i32_e32 v3, v3
	v_cvt_f32_i32_e32 v4, v4
	v_cvt_f32_i32_e32 v5, v5
	s_waitcnt vmcnt(0)
	v_fmac_f32_e32 v19, v18, v2
	v_fmac_f32_e32 v6, v18, v3
	v_fmac_f32_e32 v7, v18, v4
	v_fmac_f32_e32 v8, v18, v5
	v_cvt_pk_bf16_f32 v2, v19, v6
	v_cvt_pk_bf16_f32 v3, v7, v8
	global_store_dwordx2 v[138:139], v[2:3], off
	s_waitcnt lgkmcnt(0)
	v_lshl_add_u64 v[138:139], v[138:139], 0, s[24:25]
	s_cbranch_vccz .LBB0_1582
